# H1: unit-top vmcnt(0) replaced by counted vmcnt(20) so the previous unit's 20 stores are not drained; per-unit lower-bound loads (layer 1) hoisted out of the unit loop
# speedup vs baseline: 1.0070x; 1.0035x over previous
.LBB0_562:
	s_and_b64 vcc, exec, s[2:3]
	s_cbranch_vccnz .LBB0_649
	s_and_b32 s2, s4, 0x1fffffc0
	s_lshl_b32 s2, s2, 3
	v_readlane_b32 s3, v254, 48
	v_and_b32_e32 v23, 63, v20
	s_ashr_i32 s33, s4, 6
	s_ashr_i32 s40, s4, 7
	s_add_i32 s5, s3, s2
	v_lshlrev_b32_e32 v22, 3, v23
	s_movk_i32 s2, 0x240
	s_bitcmp1_b32 s4, 6
	v_add_u32_e32 v108, s5, v22
	v_cmp_gt_i32_e64 s[8:9], s2, v20
	v_or_b32_e32 v24, 1, v18
	v_add_u32_e32 v110, s3, v22
	s_cselect_b64 s[2:3], -1, 0
	s_addk_i32 s5, 0xfe00
	v_ashrrev_i32_e32 v25, 31, v24
	s_cmp_eq_u32 s40, 2
	s_movk_i32 s6, 0x7700
	v_lshlrev_b64 v[32:33], 11, v[24:25]
	v_or_b32_e32 v24, 2, v18
	v_add_u32_e32 v111, s5, v22
	s_cselect_b32 s5, 4, 6
	s_cselect_b32 s6, s6, 0xaa00
	s_cmp_eq_u32 s40, 1
	v_ashrrev_i32_e32 v25, 31, v24
	s_cselect_b32 s5, 2, s5
	s_cselect_b32 s6, 0x5500, s6
	s_cmpk_lt_u32 s4, 0x80
	v_lshlrev_b64 v[34:35], 11, v[24:25]
	v_or_b32_e32 v24, 3, v18
	s_cselect_b32 s34, 0, s5
	s_cselect_b32 s5, 0x4400, s6
	v_ashrrev_i32_e32 v25, 31, v24
	s_or_b32 s47, s34, 1
	s_lshl_b32 s38, s33, 3
	s_add_i32 s80, s5, 0
	v_lshlrev_b64 v[36:37], 11, v[24:25]
	v_or_b32_e32 v24, 4, v18
	s_cmp_lt_u32 s4, 64
	v_ashrrev_i32_e32 v19, 31, v18
	v_ashrrev_i32_e32 v25, 31, v24
	s_cselect_b64 s[50:51], -1, 0
	s_cmp_lt_i32 s33, 10
	v_readlane_b32 s7, v254, 49
	v_lshlrev_b64 v[30:31], 11, v[18:19]
	v_lshlrev_b64 v[38:39], 11, v[24:25]
	v_or_b32_e32 v24, 5, v18
	v_or_b32_e32 v18, 6, v18
	s_cselect_b64 s[52:53], -1, 0
	s_lshl_b32 s42, s33, 5
	s_lshl_b32 s54, s33, 4
	v_ashrrev_i32_e32 v19, 31, v18
	s_add_i32 s4, s42, s7
	s_ashr_i32 s55, s54, 31
	v_lshlrev_b64 v[42:43], 11, v[18:19]
	v_and_b32_e32 v19, 24, v22
	s_cmp_gt_i32 s40, 0
	v_add_u32_e32 v27, s4, v19
	s_cselect_b64 s[4:5], -1, 0
	s_cmp_gt_i32 s40, 1
	v_add_u32_e32 v26, s7, v2
	v_writelane_b32 v250, s8, 8
	s_cselect_b64 s[6:7], -1, 0
	s_cmp_gt_i32 s40, 2
	v_writelane_b32 v250, s9, 9
	s_cselect_b64 s[8:9], -1, 0
	s_cmp_lt_i32 s40, 1
	v_ashrrev_i32_e32 v17, 31, v16
	v_lshlrev_b32_e32 v2, 3, v20
	s_cselect_b64 s[10:11], -1, 0
	s_cmp_lt_i32 s40, 2
	v_lshlrev_b64 v[44:45], 11, v[16:17]
	v_and_b32_e32 v16, 0x78, v2
	v_lshlrev_b32_e32 v2, 2, v23
	s_cselect_b64 s[12:13], -1, 0
	s_cmp_lt_i32 s40, 3
	s_mul_i32 s39, s33, 0x880
	s_cselect_b64 s[14:15], -1, 0
	v_add_u32_e32 v116, s39, v2
	s_ashr_i32 s39, s38, 31
	s_lshl_b64 s[56:57], s[38:39], 12
	s_cmp_lt_i32 s40, 4
	s_cselect_b64 s[58:59], -1, 0
	s_or_b32 s40, s38, 1
	s_mul_i32 s39, s40, 0x110
	s_ashr_i32 s41, s40, 31
	s_lshl_b64 s[86:87], s[40:41], 12
	s_or_b32 s40, s38, 2
	s_add_i32 s41, s39, 0x110
	v_add_u32_e32 v118, s41, v2
	s_ashr_i32 s41, s40, 31
	s_lshl_b64 s[90:91], s[40:41], 12
	s_or_b32 s40, s38, 3
	s_add_i32 s41, s39, 0x220
	v_add_u32_e32 v119, s41, v2
	s_ashr_i32 s41, s40, 31
	s_lshl_b64 s[92:93], s[40:41], 12
	s_or_b32 s40, s38, 4
	s_add_i32 s41, s39, 0x330
	v_add_u32_e32 v120, s41, v2
	s_ashr_i32 s41, s40, 31
	s_lshl_b64 s[94:95], s[40:41], 12
	s_or_b32 s40, s38, 5
	s_add_i32 s41, s39, 0x440
	v_add_u32_e32 v121, s41, v2
	s_ashr_i32 s41, s40, 31
	v_add_u32_e32 v117, s39, v2
	s_lshl_b64 s[96:97], s[40:41], 12
	s_or_b32 s40, s38, 6
	s_add_i32 s41, s39, 0x550
	s_or_b32 s38, s38, 7
	s_addk_i32 s39, 0x660
	v_add_u32_e32 v123, s39, v2
	s_ashr_i32 s39, s38, 31
	s_mov_b64 s[48:49], s[20:21]
	s_lshl_b64 s[20:21], s[38:39], 12
	v_readlane_b32 s38, v251, 63
	v_readlane_b32 s39, v252, 0
	v_lshlrev_b32_e32 v107, 1, v23
	v_mov_b32_e32 v23, v3
	v_lshl_add_u64 v[50:51], s[38:39], 0, v[2:3]
	v_readlane_b32 s38, v253, 49
	v_readlane_b32 s39, v253, 50
	v_lshrrev_b32_e32 v17, 1, v20
	v_add_u32_e32 v122, s41, v2
	v_lshl_add_u64 v[52:53], s[38:39], 0, v[22:23]
	v_lshlrev_b32_e32 v2, 12, v20
	v_readlane_b32 s38, v253, 45
	v_ashrrev_i32_e32 v25, 31, v24
	v_lshlrev_b64 v[46:47], 12, v[12:13]
	v_and_b32_e32 v112, 15, v20
	v_lshrrev_b32_e32 v13, 2, v20
	v_and_b32_e32 v17, 24, v17
	v_and_b32_e32 v2, 0xf000, v2
	v_readlane_b32 s39, v253, 46
	v_lshlrev_b64 v[40:41], 11, v[24:25]
	v_and_b32_e32 v18, 12, v13
	v_and_or_b32 v13, v13, 3, v17
	v_or_b32_e32 v24, s54, v112
	v_mov_b32_e32 v25, s55
	s_movk_i32 s44, 0x110
	s_ashr_i32 s41, s40, 31
	v_lshl_add_u64 v[54:55], s[38:39], 0, v[2:3]
	v_readlane_b32 s38, v253, 47
	v_add_u32_e32 v114, 0, v19
	v_mul_u32_u24_e32 v115, 0x110, v13
	v_mul_lo_u32 v19, v12, s44
	s_lshl_b64 s[88:89], s[40:41], 12
	v_mad_u32_u24 v60, v13, s44, v235
	v_lshlrev_b64 v[12:13], 8, v[24:25]
	v_readlane_b32 s26, v250, 7
	v_readlane_b32 s39, v253, 48
	v_ashrrev_i32_e32 v15, 31, v14
	v_readlane_b32 s43, v254, 50
	s_cmp_lg_u32 s26, 0
	v_lshl_add_u64 v[12:13], s[38:39], 0, v[12:13]
	v_lshlrev_b32_e32 v2, 1, v18
	s_mul_i32 s38, s33, 0x1100
	v_lshlrev_b64 v[48:49], 12, v[14:15]
	v_and_b32_e32 v15, 48, v20
	s_cselect_b64 s[26:27], -1, 0
	v_lshl_add_u64 v[56:57], v[12:13], 0, v[2:3]
	v_mov_b32_e32 v2, s38
	s_add_i32 s38, s43, s42
	v_add_u32_e32 v59, s43, v15
	v_mul_lo_u32 v14, v14, s44
	v_mul_u32_u24_e32 v61, 0x90, v112
	v_mad_u32_u24 v2, v112, s44, v2
	v_add_u32_e32 v128, s38, v17
	v_readlane_b32 s38, v250, 3
	v_add_u32_e32 v113, 0, v15
	v_add_u32_e32 v124, 0xfffffe00, v20
	v_add_u32_e32 v125, s43, v21
	v_or_b32_e32 v126, s54, v18
	s_movk_i32 s85, 0x110
	v_add3_u32 v127, v2, v15, 0
	v_add_u32_e32 v129, v26, v19
	v_add_u32_e32 v130, v26, v14
	v_lshlrev_b32_e32 v58, 1, v16
	v_add_u32_e32 v131, v27, v115
	v_add_u32_e32 v132, v59, v61
	v_lshlrev_b32_e32 v2, 1, v18
	v_add_u32_e32 v133, v114, v60
	s_mov_b32 s82, s38
	v_readlane_b32 s39, v250, 4
	v_mov_b32_e32 v160, 0
	v_mov_b32_e32 v161, 0
	s_andn2_b64 vcc, exec, s[26:27]
	s_cbranch_vccnz .Lh1_lb_done
	s_lshl_b32 s100, s82, 5
	s_and_b32 s100, s100, 0x1e0
	s_lshl_b32 s100, s100, 2
	v_or_b32_e32 v162, s100, v107
	v_lshlrev_b32_e32 v162, 2, v162
	v_add_u32_e32 v163, 0x2000, v162
	v_readlane_b32 s100, v251, 16
	v_readlane_b32 s101, v251, 17
	s_nop 4
	global_load_dwordx2 v[160:161], v162, s[100:101]
	global_load_dwordx2 v[164:165], v163, s[100:101]
	s_waitcnt vmcnt(0)
	v_sub_f32_e32 v160, v164, v160
	v_sub_f32_e32 v161, v165, v161
	v_mul_f32_e32 v160, 0xbfb8aa3b, v160
	v_mul_f32_e32 v161, 0xbfb8aa3b, v161
	v_exp_f32_e32 v160, v160
	v_exp_f32_e32 v161, v161
	v_add_f32_e32 v160, 1.0, v160
	v_add_f32_e32 v161, 1.0, v161
	v_rcp_f32_e32 v160, v160
	v_rcp_f32_e32 v161, v161
.Lh1_lb_done:
	s_waitcnt vmcnt(0)
	s_branch .LBB0_565

.LBB0_565:
	s_lshl_b32 s38, s82, 5
	s_and_b32 s83, s38, 0x1e0
	s_andn2_b64 vcc, exec, s[26:27]
	s_lshl_b32 s42, s83, 2
	s_cbranch_vccnz .LBB0_567
	v_mov_b32_e32 v12, v160
	v_mov_b32_e32 v13, v161
	s_branch .LBB0_568

.LBB0_568:
	s_waitcnt vmcnt(20)
	v_lshlrev_b32_e32 v14, 16, v1
	v_and_b32_e32 v15, 0xffff0000, v1
	v_mul_f32_e32 v14, 0xbfb8aa3b, v14
	v_lshlrev_b32_e32 v16, 16, v29
	v_exp_f32_e32 v14, v14
	v_mul_f32_e32 v15, 0xbfb8aa3b, v15
	v_and_b32_e32 v17, 0xffff0000, v29
	v_mul_f32_e32 v16, 0xbfb8aa3b, v16
	v_lshlrev_b32_e32 v18, 16, v102
	v_exp_f32_e32 v15, v15
	v_exp_f32_e32 v16, v16
	v_mul_f32_e32 v17, 0xbfb8aa3b, v17
	v_and_b32_e32 v19, 0xffff0000, v102
	v_mul_f32_e32 v18, 0xbfb8aa3b, v18
	v_lshlrev_b32_e32 v20, 16, v103
	v_exp_f32_e32 v17, v17
	v_exp_f32_e32 v18, v18
	v_mul_f32_e32 v19, 0xbfb8aa3b, v19
	v_and_b32_e32 v21, 0xffff0000, v103
	v_mul_f32_e32 v20, 0xbfb8aa3b, v20
	v_lshlrev_b32_e32 v22, 16, v104
	v_exp_f32_e32 v19, v19
	v_exp_f32_e32 v20, v20
	v_mul_f32_e32 v21, 0xbfb8aa3b, v21
	v_and_b32_e32 v23, 0xffff0000, v104
	v_mul_f32_e32 v22, 0xbfb8aa3b, v22
	v_lshlrev_b32_e32 v24, 16, v105
	v_add_f32_e32 v14, 1.0, v14
	v_exp_f32_e32 v21, v21
	v_exp_f32_e32 v22, v22
	v_mul_f32_e32 v23, 0xbfb8aa3b, v23
	v_and_b32_e32 v25, 0xffff0000, v105
	v_mul_f32_e32 v24, 0xbfb8aa3b, v24
	v_lshlrev_b32_e32 v26, 16, v106
	v_rcp_f32_e32 v94, v14
	v_add_f32_e32 v14, 1.0, v15
	v_add_f32_e32 v16, 1.0, v16
	v_exp_f32_e32 v23, v23
	v_exp_f32_e32 v24, v24
	v_mul_f32_e32 v25, 0xbfb8aa3b, v25
	v_and_b32_e32 v27, 0xffff0000, v106
	v_mul_f32_e32 v26, 0xbfb8aa3b, v26
	v_lshlrev_b32_e32 v59, 16, v109
	v_rcp_f32_e32 v95, v14
	v_rcp_f32_e32 v82, v16
	v_add_f32_e32 v16, 1.0, v17
	v_add_f32_e32 v18, 1.0, v18
	v_exp_f32_e32 v25, v25
	v_exp_f32_e32 v26, v26
	v_mul_f32_e32 v27, 0xbfb8aa3b, v27
	v_and_b32_e32 v62, 0xffff0000, v109
	v_mul_f32_e32 v59, 0xbfb8aa3b, v59
	v_rcp_f32_e32 v83, v16
	v_rcp_f32_e32 v80, v18
	v_add_f32_e32 v18, 1.0, v19
	v_add_f32_e32 v20, 1.0, v20
	v_exp_f32_e32 v27, v27
	v_exp_f32_e32 v59, v59
	v_mul_f32_e32 v62, 0xbfb8aa3b, v62
	v_rcp_f32_e32 v81, v18
	v_rcp_f32_e32 v76, v20
	v_add_f32_e32 v20, 1.0, v21
	v_add_f32_e32 v22, 1.0, v22
	v_exp_f32_e32 v63, v62
	v_pk_add_f32 v[60:61], v[12:13], 1.0 op_sel_hi:[1,0] neg_lo:[1,0] neg_hi:[1,0]
	v_rcp_f32_e32 v77, v20
	v_rcp_f32_e32 v72, v22
	v_add_f32_e32 v22, 1.0, v23
	v_add_f32_e32 v24, 1.0, v24
	v_pk_fma_f32 v[14:15], v[94:95], v[60:61], v[12:13]
	v_rcp_f32_e32 v73, v22
	v_rcp_f32_e32 v68, v24
	v_add_f32_e32 v24, 1.0, v25
	v_add_f32_e32 v26, 1.0, v26
	v_max_f32_e32 v14, 0xda24260, v14
	v_max_f32_e32 v15, 0xda24260, v15
	v_pk_fma_f32 v[16:17], v[82:83], v[60:61], v[12:13]
	v_rcp_f32_e32 v69, v24
	v_rcp_f32_e32 v66, v26
	v_add_f32_e32 v26, 1.0, v27
	v_add_f32_e32 v59, 1.0, v59
	v_log_f32_e32 v14, v14
	v_log_f32_e32 v15, v15
	v_max_f32_e32 v16, 0xda24260, v16
	v_max_f32_e32 v17, 0xda24260, v17
	v_pk_fma_f32 v[18:19], v[80:81], v[60:61], v[12:13]
	v_rcp_f32_e32 v67, v26
	v_rcp_f32_e32 v62, v59
	v_add_f32_e32 v59, 1.0, v63
	v_log_f32_e32 v16, v16
	v_log_f32_e32 v17, v17
	v_max_f32_e32 v18, 0xda24260, v18
	v_max_f32_e32 v19, 0xda24260, v19
	v_pk_fma_f32 v[20:21], v[76:77], v[60:61], v[12:13]
	v_rcp_f32_e32 v63, v59
	v_log_f32_e32 v18, v18
	v_log_f32_e32 v19, v19
	v_max_f32_e32 v20, 0xda24260, v20
	v_max_f32_e32 v21, 0xda24260, v21
	v_pk_fma_f32 v[22:23], v[72:73], v[60:61], v[12:13]
	v_log_f32_e32 v20, v20
	v_log_f32_e32 v21, v21
	v_max_f32_e32 v22, 0xda24260, v22
	v_max_f32_e32 v23, 0xda24260, v23
	v_pk_fma_f32 v[24:25], v[68:69], v[60:61], v[12:13]
	v_log_f32_e32 v22, v22
	v_log_f32_e32 v23, v23
	v_max_f32_e32 v24, 0xda24260, v24
	v_max_f32_e32 v25, 0xda24260, v25
	v_pk_fma_f32 v[26:27], v[66:67], v[60:61], v[12:13]
	v_pk_add_f32 v[96:97], v[14:15], 0 op_sel_hi:[1,0]
	v_log_f32_e32 v24, v24
	v_log_f32_e32 v25, v25
	v_max_f32_e32 v26, 0xda24260, v26
	v_max_f32_e32 v27, 0xda24260, v27
	v_pk_fma_f32 v[12:13], v[62:63], v[60:61], v[12:13]
	v_pk_add_f32 v[98:99], v[16:17], v[96:97]
	v_log_f32_e32 v26, v26
	v_log_f32_e32 v27, v27
	v_max_f32_e32 v12, 0xda24260, v12
	v_max_f32_e32 v13, 0xda24260, v13
	v_pk_add_f32 v[92:93], v[18:19], v[98:99]
	v_log_f32_e32 v12, v12
	v_log_f32_e32 v13, v13
	v_pk_add_f32 v[88:89], v[20:21], v[92:93]
	s_nop 0
	v_pk_add_f32 v[78:79], v[22:23], v[88:89]
	s_nop 0
	v_pk_add_f32 v[74:75], v[24:25], v[78:79]
	s_nop 0
	v_pk_add_f32 v[70:71], v[26:27], v[74:75]
	s_nop 0
	v_pk_add_f32 v[64:65], v[12:13], v[70:71]
	ds_write_b64 v108, v[64:65]
	ds_write_b128 v129, v[4:7]
	ds_write_b128 v130, v[8:11]
	s_mov_b64 s[38:39], exec
	v_readlane_b32 s40, v250, 8
	v_readlane_b32 s41, v250, 9
	s_and_b64 s[40:41], s[38:39], s[40:41]
	s_mov_b64 exec, s[40:41]
	s_cbranch_execz .LBB0_571
	s_mov_b64 s[40:41], 0
	v_mov_b32_e32 v12, v125
	v_mov_b32_e32 v13, v124
